# v028 + phase A: per-k-step LDS waits merged into one wait before first MFMA
# speedup vs baseline: 1.0283x; 1.0040x over previous
.LBB3_12:
	s_or_b64 exec, exec, s[10:11]
	v_or_b32_e32 v3, v51, v1
	v_lshlrev_b32_e32 v166, 6, v3
	v_or_b32_e32 v167, 0x300, v166
	v_or_b32_e32 v3, v162, v167
	v_lshlrev_b32_e32 v3, 4, v3
	v_or_b32_e32 v35, v163, v167
	v_lshlrev_b32_e32 v35, 4, v35
	global_load_dwordx4 v[114:117], v3, s[8:9]
	global_load_dwordx4 v[118:121], v35, s[8:9]
	v_or_b32_e32 v3, v164, v167
	v_lshlrev_b32_e32 v3, 4, v3
	global_load_dwordx4 v[122:125], v3, s[8:9]
	v_mul_u32_u24_e32 v3, 0x3000, v208
	v_or_b32_e32 v161, v3, v202
	v_add_u32_e32 v165, v150, v202
	ds_read_b128 v[152:155], v161
	ds_read_b128 v[146:149], v161 offset:4096
	ds_read_b128 v[142:145], v161 offset:8192
	s_waitcnt vmcnt(16)
	ds_write_b128 v165, v[126:129] offset:24576
	s_waitcnt vmcnt(15)
	ds_write_b128 v165, v[130:133] offset:32768
	s_waitcnt vmcnt(14)
	ds_write_b128 v165, v[134:137] offset:40960
	ds_read_b128 v[138:141], v161 offset:1024
	ds_read_b128 v[130:133], v161 offset:5120
	ds_read_b128 v[126:129], v161 offset:9216
	v_mov_b32_e32 v3, v50
	v_mov_b32_e32 v35, v52
	s_waitcnt lgkmcnt(6)
	v_mfma_f32_32x32x16_bf16 v[18:33], v[152:155], v[110:113], v[18:33]
	s_cmp_lg_u64 s[4:5], 0
	s_cbranch_scc0 .LBB3_14
	v_mfma_f32_32x32x16_bf16 v[2:17], v[110:113], v[146:149], v[2:17]
	v_mfma_f32_32x32x16_bf16 v[34:49], v[110:113], v[142:145], v[34:49]
	s_branch .LBB3_16
.LBB3_14:
	v_mfma_f32_32x32x16_bf16 v[2:17], v[146:149], v[110:113], v[2:17]
	v_mfma_f32_32x32x16_bf16 v[34:49], v[142:145], v[110:113], v[34:49]
.LBB3_16:
	ds_read_b128 v[134:137], v161 offset:2048
	ds_read_b128 v[110:113], v161 offset:6144
	ds_read_b128 v[50:53], v161 offset:10240
	s_waitcnt lgkmcnt(3)
	v_mfma_f32_32x32x16_bf16 v[18:33], v[138:141], v[94:97], v[18:33]
	s_cmp_lg_u64 s[4:5], 0
	s_cbranch_scc0 .LBB3_18
	v_mfma_f32_32x32x16_bf16 v[2:17], v[94:97], v[130:133], v[2:17]
	v_mfma_f32_32x32x16_bf16 v[34:49], v[94:97], v[126:129], v[34:49]
	s_branch .LBB3_20
.LBB3_18:
	v_mfma_f32_32x32x16_bf16 v[2:17], v[130:133], v[94:97], v[2:17]
	v_mfma_f32_32x32x16_bf16 v[34:49], v[126:129], v[94:97], v[34:49]
.LBB3_20:
	s_waitcnt lgkmcnt(3)
	s_barrier
	s_waitcnt lgkmcnt(4)
	ds_read_b128 v[130:133], v161 offset:3072
	s_waitcnt lgkmcnt(4)
	ds_read_b128 v[126:129], v161 offset:7168
	ds_read_b128 v[94:97], v161 offset:11264
	s_waitcnt lgkmcnt(3)
	v_mfma_f32_32x32x16_bf16 v[18:33], v[134:137], v[90:93], v[18:33]
	s_cmp_lg_u64 s[4:5], 0
	s_cbranch_scc0 .LBB3_22
	v_mfma_f32_32x32x16_bf16 v[2:17], v[90:93], v[110:113], v[2:17]
	v_mfma_f32_32x32x16_bf16 v[34:49], v[90:93], v[50:53], v[34:49]
	s_branch .LBB3_24
.LBB3_22:
	v_mfma_f32_32x32x16_bf16 v[2:17], v[110:113], v[90:93], v[2:17]
	v_mfma_f32_32x32x16_bf16 v[34:49], v[50:53], v[90:93], v[34:49]
.LBB3_24:
	ds_read_b128 v[138:141], v161 offset:28672
	ds_read_b128 v[142:145], v161 offset:24576
	ds_read_b128 v[134:137], v161 offset:32768
	s_waitcnt lgkmcnt(3)
	v_mfma_f32_32x32x16_bf16 v[18:33], v[130:133], v[86:89], v[18:33]
	s_cmp_lg_u64 s[4:5], 0
	s_cbranch_scc0 .LBB3_26
	v_mfma_f32_32x32x16_bf16 v[2:17], v[86:89], v[126:129], v[2:17]
	v_mfma_f32_32x32x16_bf16 v[34:49], v[86:89], v[94:97], v[34:49]
	s_branch .LBB3_28
.LBB3_26:
	v_mfma_f32_32x32x16_bf16 v[2:17], v[126:129], v[86:89], v[2:17]
	v_mfma_f32_32x32x16_bf16 v[34:49], v[94:97], v[86:89], v[34:49]
.LBB3_28:
	v_add_co_u32_e32 v50, vcc, 0x3000, v158
	s_nop 1
	v_addc_co_u32_e32 v51, vcc, 0, v159, vcc
	s_waitcnt lgkmcnt(3)
	global_load_dwordx4 v[94:97], v[50:51], off
	global_load_dwordx4 v[90:93], v[50:51], off offset:1024
	global_load_dwordx4 v[86:89], v[50:51], off offset:2048
	s_nop 0
	global_load_dwordx4 v[50:53], v[50:51], off offset:3072
	v_add_u32_e32 v130, 0x100, v167
	v_or_b32_e32 v110, v162, v130
	v_or_b32_e32 v111, v163, v130
	v_or_b32_e32 v130, v164, v130
	v_lshlrev_b32_e32 v110, 4, v110
	v_lshlrev_b32_e32 v126, 4, v111
	v_lshlrev_b32_e32 v130, 4, v130
	global_load_dwordx4 v[110:113], v110, s[8:9]
	s_nop 0
	global_load_dwordx4 v[126:129], v126, s[8:9]
	s_nop 0
	global_load_dwordx4 v[130:133], v130, s[8:9]
	s_waitcnt vmcnt(12)
	ds_write_b128 v165, v[98:101] offset:49152
	s_waitcnt vmcnt(11)
	ds_write_b128 v165, v[102:105] offset:57344
	v_or_b32_e32 v98, 0x10000, v150
	v_add_u32_e32 v168, v98, v202
	s_waitcnt vmcnt(10)
	ds_write_b128 v168, v[106:109]
	ds_read_b128 v[106:109], v161 offset:29696
	ds_read_b128 v[146:149], v161 offset:25600
	ds_read_b128 v[102:105], v161 offset:33792
	s_waitcnt lgkmcnt(6)
	v_mfma_f32_32x32x16_bf16 v[18:33], v[142:145], v[82:85], v[18:33]
	s_cmp_lg_u64 s[4:5], 0
	s_cbranch_scc0 .LBB3_30
	v_mfma_f32_32x32x16_bf16 v[2:17], v[82:85], v[138:141], v[2:17]
	v_mfma_f32_32x32x16_bf16 v[34:49], v[82:85], v[134:137], v[34:49]
	s_branch .LBB3_32
.LBB3_30:
	v_mfma_f32_32x32x16_bf16 v[2:17], v[138:141], v[82:85], v[2:17]
	v_mfma_f32_32x32x16_bf16 v[34:49], v[134:137], v[82:85], v[34:49]
.LBB3_32:
	ds_read_b128 v[98:101], v161 offset:30720
	s_waitcnt lgkmcnt(7)
	ds_read_b128 v[134:137], v161 offset:26624
	ds_read_b128 v[82:85], v161 offset:34816
	s_waitcnt lgkmcnt(3)
	v_mfma_f32_32x32x16_bf16 v[18:33], v[146:149], v[78:81], v[18:33]
	s_cmp_lg_u64 s[4:5], 0
	s_cbranch_scc0 .LBB3_34
	v_mfma_f32_32x32x16_bf16 v[2:17], v[78:81], v[106:109], v[2:17]
	v_mfma_f32_32x32x16_bf16 v[34:49], v[78:81], v[102:105], v[34:49]
	s_branch .LBB3_36
.LBB3_34:
	v_mfma_f32_32x32x16_bf16 v[2:17], v[106:109], v[78:81], v[2:17]
	v_mfma_f32_32x32x16_bf16 v[34:49], v[102:105], v[78:81], v[34:49]
.LBB3_36:
	s_waitcnt lgkmcnt(3)
	s_barrier
	ds_read_b128 v[106:109], v161 offset:31744
	ds_read_b128 v[138:141], v161 offset:27648
	ds_read_b128 v[78:81], v161 offset:35840
	s_waitcnt lgkmcnt(3)
	v_mfma_f32_32x32x16_bf16 v[18:33], v[134:137], v[74:77], v[18:33]
	s_cmp_lg_u64 s[4:5], 0
	s_cbranch_scc0 .LBB3_38
	v_mfma_f32_32x32x16_bf16 v[2:17], v[74:77], v[98:101], v[2:17]
	v_mfma_f32_32x32x16_bf16 v[34:49], v[74:77], v[82:85], v[34:49]
	s_branch .LBB3_40
.LBB3_38:
	v_mfma_f32_32x32x16_bf16 v[2:17], v[98:101], v[74:77], v[2:17]
	v_mfma_f32_32x32x16_bf16 v[34:49], v[82:85], v[74:77], v[34:49]
.LBB3_40:
	ds_read_b128 v[150:153], v161 offset:49152
	ds_read_b128 v[102:105], v161 offset:53248
	s_waitcnt lgkmcnt(5)
	ds_read_b128 v[82:85], v161 offset:57344
	s_waitcnt lgkmcnt(3)
	v_mfma_f32_32x32x16_bf16 v[18:33], v[138:141], v[70:73], v[18:33]
	s_cmp_lg_u64 s[4:5], 0
	s_cbranch_scc0 .LBB3_42
	v_mfma_f32_32x32x16_bf16 v[2:17], v[70:73], v[106:109], v[2:17]
	v_mfma_f32_32x32x16_bf16 v[34:49], v[70:73], v[78:81], v[34:49]
	s_branch .LBB3_44
.LBB3_42:
	v_mfma_f32_32x32x16_bf16 v[2:17], v[106:109], v[70:73], v[2:17]
	v_mfma_f32_32x32x16_bf16 v[34:49], v[78:81], v[70:73], v[34:49]
.LBB3_44:
	v_add_co_u32_e32 v70, vcc, 0x4000, v158
	s_nop 1
	v_addc_co_u32_e32 v71, vcc, 0, v159, vcc
	global_load_dwordx4 v[98:101], v[70:71], off
	s_waitcnt lgkmcnt(3)
	global_load_dwordx4 v[78:81], v[70:71], off offset:1024
	global_load_dwordx4 v[74:77], v[70:71], off offset:2048
	s_nop 0
	global_load_dwordx4 v[70:73], v[70:71], off offset:3072
	v_add_u32_e32 v138, 0x200, v167
	v_or_b32_e32 v106, v162, v138
	v_or_b32_e32 v107, v163, v138
	v_or_b32_e32 v138, v164, v138
	v_lshlrev_b32_e32 v106, 4, v106
	v_lshlrev_b32_e32 v134, 4, v107
	v_lshlrev_b32_e32 v138, 4, v138
	global_load_dwordx4 v[106:109], v106, s[8:9]
	s_nop 0
	global_load_dwordx4 v[134:137], v134, s[8:9]
	s_nop 0
	global_load_dwordx4 v[138:141], v138, s[8:9]
	ds_read_b128 v[154:157], v161 offset:50176
	ds_read_b128 v[146:149], v161 offset:54272
	ds_read_b128 v[142:145], v161 offset:58368
	s_waitcnt vmcnt(16)
	ds_write_b128 v165, v[114:117]
	s_waitcnt vmcnt(15)
	ds_write_b128 v165, v[118:121] offset:8192
	s_waitcnt vmcnt(14)
	ds_write_b128 v165, v[122:125] offset:16384
	s_waitcnt lgkmcnt(6)
	v_mfma_f32_32x32x16_bf16 v[18:33], v[150:153], v[66:69], v[18:33]
	s_cmp_lg_u64 s[4:5], 0
	s_cbranch_scc0 .LBB3_46
	v_mfma_f32_32x32x16_bf16 v[2:17], v[66:69], v[102:105], v[2:17]
	v_mfma_f32_32x32x16_bf16 v[34:49], v[66:69], v[82:85], v[34:49]
	s_branch .LBB3_48
.LBB3_46:
	v_mfma_f32_32x32x16_bf16 v[2:17], v[102:105], v[66:69], v[2:17]
	v_mfma_f32_32x32x16_bf16 v[34:49], v[82:85], v[66:69], v[34:49]
.LBB3_48:
	ds_read_b128 v[114:117], v161 offset:51200
	s_waitcnt lgkmcnt(7)
	ds_read_b128 v[82:85], v161 offset:55296
	ds_read_b128 v[66:69], v161 offset:59392
	s_waitcnt lgkmcnt(6)
	v_mfma_f32_32x32x16_bf16 v[18:33], v[154:157], v[62:65], v[18:33]
	s_cmp_lg_u64 s[4:5], 0
	s_cbranch_scc0 .LBB3_50
	v_mfma_f32_32x32x16_bf16 v[2:17], v[62:65], v[146:149], v[2:17]
	v_mfma_f32_32x32x16_bf16 v[34:49], v[62:65], v[142:145], v[34:49]
	s_branch .LBB3_52
.LBB3_50:
	v_mfma_f32_32x32x16_bf16 v[2:17], v[146:149], v[62:65], v[2:17]
	v_mfma_f32_32x32x16_bf16 v[34:49], v[142:145], v[62:65], v[34:49]
.LBB3_52:
	s_waitcnt lgkmcnt(3)
	s_barrier
	ds_read_b128 v[118:121], v161 offset:52224
	ds_read_b128 v[102:105], v161 offset:56320
	ds_read_b128 v[62:65], v161 offset:60416
	s_waitcnt lgkmcnt(3)
	v_mfma_f32_32x32x16_bf16 v[18:33], v[114:117], v[58:61], v[18:33]
	s_cmp_lg_u64 s[4:5], 0
	s_cbranch_scc0 .LBB3_54
	v_mfma_f32_32x32x16_bf16 v[2:17], v[58:61], v[82:85], v[2:17]
	v_mfma_f32_32x32x16_bf16 v[34:49], v[58:61], v[66:69], v[34:49]
	s_branch .LBB3_56
.LBB3_54:
	v_mfma_f32_32x32x16_bf16 v[2:17], v[82:85], v[58:61], v[2:17]
	v_mfma_f32_32x32x16_bf16 v[34:49], v[66:69], v[58:61], v[34:49]
.LBB3_56:
	ds_read_b128 v[142:145], v161
	s_waitcnt lgkmcnt(4)
	ds_read_b128 v[66:69], v161 offset:4096
	ds_read_b128 v[58:61], v161 offset:8192
	s_waitcnt lgkmcnt(3)
	v_mfma_f32_32x32x16_bf16 v[18:33], v[118:121], v[54:57], v[18:33]
	s_cmp_lg_u64 s[4:5], 0
	s_cbranch_scc0 .LBB3_58
	v_mfma_f32_32x32x16_bf16 v[2:17], v[54:57], v[102:105], v[2:17]
	v_mfma_f32_32x32x16_bf16 v[34:49], v[54:57], v[62:65], v[34:49]
	s_branch .LBB3_60
.LBB3_58:
	v_mfma_f32_32x32x16_bf16 v[2:17], v[102:105], v[54:57], v[2:17]
	v_mfma_f32_32x32x16_bf16 v[34:49], v[62:65], v[54:57], v[34:49]
.LBB3_60:
	v_add_co_u32_e32 v54, vcc, 0x5000, v158
	s_nop 1
	v_addc_co_u32_e32 v55, vcc, 0, v159, vcc
	s_waitcnt lgkmcnt(4)
	global_load_dwordx4 v[102:105], v[54:55], off
	global_load_dwordx4 v[82:85], v[54:55], off offset:1024
	s_waitcnt lgkmcnt(3)
	global_load_dwordx4 v[62:65], v[54:55], off offset:2048
	s_nop 0
	global_load_dwordx4 v[54:57], v[54:55], off offset:3072
	v_add_u32_e32 v122, 0x300, v167
	v_or_b32_e32 v114, v162, v122
	v_or_b32_e32 v115, v163, v122
	v_or_b32_e32 v122, v164, v122
	v_lshlrev_b32_e32 v114, 4, v114
	v_lshlrev_b32_e32 v118, 4, v115
	v_lshlrev_b32_e32 v122, 4, v122
	global_load_dwordx4 v[114:117], v114, s[8:9]
	s_nop 0
	global_load_dwordx4 v[118:121], v118, s[8:9]
	s_nop 0
	global_load_dwordx4 v[122:125], v122, s[8:9]
	s_waitcnt vmcnt(16)
	ds_write_b128 v165, v[110:113] offset:24576
	s_waitcnt vmcnt(15)
	ds_write_b128 v165, v[126:129] offset:32768
	s_waitcnt vmcnt(14)
	ds_write_b128 v165, v[130:133] offset:40960
	ds_read_b128 v[146:149], v161 offset:1024
	ds_read_b128 v[126:129], v161 offset:5120
	ds_read_b128 v[110:113], v161 offset:9216
	s_waitcnt lgkmcnt(6)
	v_mfma_f32_32x32x16_bf16 v[18:33], v[142:145], v[94:97], v[18:33]
	s_cmp_lg_u64 s[4:5], 0
	s_cbranch_scc0 .LBB3_62
	v_mfma_f32_32x32x16_bf16 v[2:17], v[94:97], v[66:69], v[2:17]
	v_mfma_f32_32x32x16_bf16 v[34:49], v[94:97], v[58:61], v[34:49]
	s_branch .LBB3_64
.LBB3_62:
	v_mfma_f32_32x32x16_bf16 v[2:17], v[66:69], v[94:97], v[2:17]
	v_mfma_f32_32x32x16_bf16 v[34:49], v[58:61], v[94:97], v[34:49]
.LBB3_64:
	ds_read_b128 v[130:133], v161 offset:2048
	ds_read_b128 v[94:97], v161 offset:6144
	s_waitcnt lgkmcnt(8)
	ds_read_b128 v[58:61], v161 offset:10240
	s_waitcnt lgkmcnt(3)
	v_mfma_f32_32x32x16_bf16 v[18:33], v[146:149], v[90:93], v[18:33]
	s_cmp_lg_u64 s[4:5], 0
	s_cbranch_scc0 .LBB3_66
	v_mfma_f32_32x32x16_bf16 v[2:17], v[90:93], v[126:129], v[2:17]
	v_mfma_f32_32x32x16_bf16 v[34:49], v[90:93], v[110:113], v[34:49]
	s_branch .LBB3_68
.LBB3_66:
	v_mfma_f32_32x32x16_bf16 v[2:17], v[126:129], v[90:93], v[2:17]
	v_mfma_f32_32x32x16_bf16 v[34:49], v[110:113], v[90:93], v[34:49]
.LBB3_68:
	s_waitcnt lgkmcnt(3)
	s_barrier
	s_waitcnt lgkmcnt(3)
	ds_read_b128 v[110:113], v161 offset:3072
	ds_read_b128 v[90:93], v161 offset:7168
	ds_read_b128 v[66:69], v161 offset:11264
	s_waitcnt lgkmcnt(3)
	v_mfma_f32_32x32x16_bf16 v[18:33], v[130:133], v[86:89], v[18:33]
	s_cmp_lg_u64 s[4:5], 0
	s_cbranch_scc0 .LBB3_70
	v_mfma_f32_32x32x16_bf16 v[2:17], v[86:89], v[94:97], v[2:17]
	v_mfma_f32_32x32x16_bf16 v[34:49], v[86:89], v[58:61], v[34:49]
	s_branch .LBB3_72
.LBB3_70:
	v_mfma_f32_32x32x16_bf16 v[2:17], v[94:97], v[86:89], v[2:17]
	v_mfma_f32_32x32x16_bf16 v[34:49], v[58:61], v[86:89], v[34:49]
.LBB3_72:
	ds_read_b128 v[130:133], v161 offset:28672
	ds_read_b128 v[142:145], v161 offset:24576
	s_waitcnt lgkmcnt(5)
	ds_read_b128 v[58:61], v161 offset:32768
	s_waitcnt lgkmcnt(3)
	v_mfma_f32_32x32x16_bf16 v[18:33], v[110:113], v[50:53], v[18:33]
	s_cmp_lg_u64 s[4:5], 0
	s_cbranch_scc0 .LBB3_74
	v_mfma_f32_32x32x16_bf16 v[2:17], v[50:53], v[90:93], v[2:17]
	v_mfma_f32_32x32x16_bf16 v[34:49], v[50:53], v[66:69], v[34:49]
	s_branch .LBB3_76
.LBB3_74:
	v_mfma_f32_32x32x16_bf16 v[2:17], v[90:93], v[50:53], v[2:17]
	v_mfma_f32_32x32x16_bf16 v[34:49], v[66:69], v[50:53], v[34:49]
.LBB3_76:
	v_add_co_u32_e32 v50, vcc, 0x6000, v158
	s_nop 1
	v_addc_co_u32_e32 v51, vcc, 0, v159, vcc
	s_waitcnt lgkmcnt(4)
	global_load_dwordx4 v[90:93], v[50:51], off
	global_load_dwordx4 v[86:89], v[50:51], off offset:1024
	s_waitcnt lgkmcnt(3)
	global_load_dwordx4 v[66:69], v[50:51], off offset:2048
	s_nop 0
	global_load_dwordx4 v[50:53], v[50:51], off offset:3072
	v_or_b32_e32 v126, 0x700, v166
	v_or_b32_e32 v94, v162, v126
	v_or_b32_e32 v95, v163, v126
	v_or_b32_e32 v126, v164, v126
	v_lshlrev_b32_e32 v94, 4, v94
	v_lshlrev_b32_e32 v110, 4, v95
	v_lshlrev_b32_e32 v126, 4, v126
	global_load_dwordx4 v[94:97], v94, s[8:9]
	s_nop 0
	global_load_dwordx4 v[110:113], v110, s[8:9]
	s_nop 0
	global_load_dwordx4 v[126:129], v126, s[8:9]
	s_waitcnt vmcnt(16)
	ds_write_b128 v165, v[106:109] offset:49152
	s_waitcnt vmcnt(15)
	ds_write_b128 v165, v[134:137] offset:57344
	s_waitcnt vmcnt(14)
	ds_write_b128 v168, v[138:141]
	ds_read_b128 v[134:137], v161 offset:29696
	ds_read_b128 v[146:149], v161 offset:25600
	ds_read_b128 v[106:109], v161 offset:33792
	s_waitcnt lgkmcnt(6)
	v_mfma_f32_32x32x16_bf16 v[18:33], v[142:145], v[98:101], v[18:33]
	s_cmp_lg_u64 s[4:5], 0
	s_cbranch_scc0 .LBB3_78
	v_mfma_f32_32x32x16_bf16 v[2:17], v[98:101], v[130:133], v[2:17]
	v_mfma_f32_32x32x16_bf16 v[34:49], v[98:101], v[58:61], v[34:49]
	s_branch .LBB3_80
.LBB3_78:
	v_mfma_f32_32x32x16_bf16 v[2:17], v[130:133], v[98:101], v[2:17]
	v_mfma_f32_32x32x16_bf16 v[34:49], v[58:61], v[98:101], v[34:49]
.LBB3_80:
	ds_read_b128 v[98:101], v161 offset:30720
	ds_read_b128 v[138:141], v161 offset:26624
	s_waitcnt lgkmcnt(8)
	ds_read_b128 v[58:61], v161 offset:34816
	s_waitcnt lgkmcnt(3)
	v_mfma_f32_32x32x16_bf16 v[18:33], v[146:149], v[78:81], v[18:33]
	s_cmp_lg_u64 s[4:5], 0
	s_cbranch_scc0 .LBB3_82
	v_mfma_f32_32x32x16_bf16 v[2:17], v[78:81], v[134:137], v[2:17]
	v_mfma_f32_32x32x16_bf16 v[34:49], v[78:81], v[106:109], v[34:49]
	s_branch .LBB3_84
.LBB3_82:
	v_mfma_f32_32x32x16_bf16 v[2:17], v[134:137], v[78:81], v[2:17]
	v_mfma_f32_32x32x16_bf16 v[34:49], v[106:109], v[78:81], v[34:49]
.LBB3_84:
	s_waitcnt lgkmcnt(3)
	s_barrier
	ds_read_b128 v[130:133], v161 offset:31744
	ds_read_b128 v[134:137], v161 offset:27648
	ds_read_b128 v[78:81], v161 offset:35840
	s_waitcnt lgkmcnt(3)
	v_mfma_f32_32x32x16_bf16 v[18:33], v[138:141], v[74:77], v[18:33]
	s_cmp_lg_u64 s[4:5], 0
	s_cbranch_scc0 .LBB3_86
	v_mfma_f32_32x32x16_bf16 v[2:17], v[74:77], v[98:101], v[2:17]
	v_mfma_f32_32x32x16_bf16 v[34:49], v[74:77], v[58:61], v[34:49]
	s_branch .LBB3_88
.LBB3_86:
	v_mfma_f32_32x32x16_bf16 v[2:17], v[98:101], v[74:77], v[2:17]
	v_mfma_f32_32x32x16_bf16 v[34:49], v[58:61], v[74:77], v[34:49]
.LBB3_88:
	ds_read_b128 v[138:141], v161 offset:49152
	ds_read_b128 v[106:109], v161 offset:53248
	ds_read_b128 v[98:101], v161 offset:57344
	s_waitcnt lgkmcnt(3)
	v_mfma_f32_32x32x16_bf16 v[18:33], v[134:137], v[70:73], v[18:33]
	s_cmp_lg_u64 s[4:5], 0
	s_cbranch_scc0 .LBB3_90
	v_mfma_f32_32x32x16_bf16 v[2:17], v[70:73], v[130:133], v[2:17]
	v_mfma_f32_32x32x16_bf16 v[34:49], v[70:73], v[78:81], v[34:49]
	s_branch .LBB3_92
.LBB3_90:
	v_mfma_f32_32x32x16_bf16 v[2:17], v[130:133], v[70:73], v[2:17]
	v_mfma_f32_32x32x16_bf16 v[34:49], v[78:81], v[70:73], v[34:49]
.LBB3_92:
	v_add_co_u32_e32 v58, vcc, 0x7000, v158
	s_nop 1
	v_addc_co_u32_e32 v59, vcc, 0, v159, vcc
	s_waitcnt lgkmcnt(3)
	global_load_dwordx4 v[78:81], v[58:59], off
	global_load_dwordx4 v[74:77], v[58:59], off offset:1024
	global_load_dwordx4 v[70:73], v[58:59], off offset:2048
	s_nop 0
	global_load_dwordx4 v[58:61], v[58:59], off offset:3072
	ds_read_b128 v[142:145], v161 offset:50176
	ds_read_b128 v[134:137], v161 offset:54272
	ds_read_b128 v[130:133], v161 offset:58368
	s_waitcnt vmcnt(13)
	ds_write_b128 v165, v[114:117]
	s_waitcnt vmcnt(12)
	ds_write_b128 v165, v[118:121] offset:8192
	s_waitcnt vmcnt(11)
	ds_write_b128 v165, v[122:125] offset:16384
	s_waitcnt lgkmcnt(6)
	v_mfma_f32_32x32x16_bf16 v[18:33], v[138:141], v[102:105], v[18:33]
	s_cmp_lg_u64 s[4:5], 0
	s_cbranch_scc0 .LBB3_94
	v_mfma_f32_32x32x16_bf16 v[2:17], v[102:105], v[106:109], v[2:17]
	v_mfma_f32_32x32x16_bf16 v[34:49], v[102:105], v[98:101], v[34:49]
	s_branch .LBB3_96
.LBB3_94:
	v_mfma_f32_32x32x16_bf16 v[2:17], v[106:109], v[102:105], v[2:17]
	v_mfma_f32_32x32x16_bf16 v[34:49], v[98:101], v[102:105], v[34:49]
.LBB3_96:
	ds_read_b128 v[114:117], v161 offset:51200
	ds_read_b128 v[102:105], v161 offset:55296
	s_waitcnt lgkmcnt(8)
	ds_read_b128 v[98:101], v161 offset:59392
	s_waitcnt lgkmcnt(6)
	v_mfma_f32_32x32x16_bf16 v[18:33], v[142:145], v[82:85], v[18:33]
	s_cmp_lg_u64 s[4:5], 0
	s_cbranch_scc0 .LBB3_98
	v_mfma_f32_32x32x16_bf16 v[2:17], v[82:85], v[134:137], v[2:17]
	v_mfma_f32_32x32x16_bf16 v[34:49], v[82:85], v[130:133], v[34:49]
	s_branch .LBB3_100
.LBB3_98:
	v_mfma_f32_32x32x16_bf16 v[2:17], v[134:137], v[82:85], v[2:17]
	v_mfma_f32_32x32x16_bf16 v[34:49], v[130:133], v[82:85], v[34:49]
.LBB3_100:
	s_waitcnt lgkmcnt(3)
	s_barrier
	ds_read_b128 v[118:121], v161 offset:52224
	ds_read_b128 v[106:109], v161 offset:56320
	ds_read_b128 v[82:85], v161 offset:60416
	s_waitcnt lgkmcnt(3)
	v_mfma_f32_32x32x16_bf16 v[18:33], v[114:117], v[62:65], v[18:33]
	s_cmp_lg_u64 s[4:5], 0
	s_cbranch_scc0 .LBB3_102
	v_mfma_f32_32x32x16_bf16 v[2:17], v[62:65], v[102:105], v[2:17]
	v_mfma_f32_32x32x16_bf16 v[34:49], v[62:65], v[98:101], v[34:49]
	s_branch .LBB3_104
.LBB3_102:
	v_mfma_f32_32x32x16_bf16 v[2:17], v[102:105], v[62:65], v[2:17]
	v_mfma_f32_32x32x16_bf16 v[34:49], v[98:101], v[62:65], v[34:49]
.LBB3_104:
	s_waitcnt lgkmcnt(4)
	ds_read_b128 v[102:105], v161
	s_waitcnt lgkmcnt(4)
	ds_read_b128 v[98:101], v161 offset:4096
	ds_read_b128 v[62:65], v161 offset:8192
	s_waitcnt lgkmcnt(3)
	v_mfma_f32_32x32x16_bf16 v[18:33], v[118:121], v[54:57], v[18:33]
	s_cmp_lg_u64 s[4:5], 0
	s_cbranch_scc0 .LBB3_106
	v_mfma_f32_32x32x16_bf16 v[2:17], v[54:57], v[106:109], v[2:17]
	v_mfma_f32_32x32x16_bf16 v[34:49], v[54:57], v[82:85], v[34:49]
	s_branch .LBB3_108
.LBB3_106:
	v_mfma_f32_32x32x16_bf16 v[2:17], v[106:109], v[54:57], v[2:17]
	v_mfma_f32_32x32x16_bf16 v[34:49], v[82:85], v[54:57], v[34:49]
.LBB3_108:
	s_waitcnt vmcnt(6)
	ds_write_b128 v165, v[94:97] offset:24576
	s_waitcnt vmcnt(5)
	ds_write_b128 v165, v[110:113] offset:32768
	s_waitcnt vmcnt(4)
	ds_write_b128 v165, v[126:129] offset:40960
	s_waitcnt lgkmcnt(7)
	ds_read_b128 v[106:109], v161 offset:1024
	ds_read_b128 v[94:97], v161 offset:5120
	s_waitcnt lgkmcnt(8)
	ds_read_b128 v[82:85], v161 offset:9216
	s_waitcnt lgkmcnt(6)
	v_mfma_f32_32x32x16_bf16 v[18:33], v[102:105], v[90:93], v[18:33]
	s_cmp_lg_u64 s[4:5], 0
	s_cbranch_scc0 .LBB3_110
	v_mfma_f32_32x32x16_bf16 v[2:17], v[90:93], v[98:101], v[2:17]
	v_mfma_f32_32x32x16_bf16 v[34:49], v[90:93], v[62:65], v[34:49]
	s_branch .LBB3_112
.LBB3_110:
	v_mfma_f32_32x32x16_bf16 v[2:17], v[98:101], v[90:93], v[2:17]
	v_mfma_f32_32x32x16_bf16 v[34:49], v[62:65], v[90:93], v[34:49]
.LBB3_112:
	s_waitcnt lgkmcnt(7)
	ds_read_b128 v[98:101], v161 offset:2048
	ds_read_b128 v[90:93], v161 offset:6144
	ds_read_b128 v[54:57], v161 offset:10240
	s_waitcnt lgkmcnt(3)
	v_mfma_f32_32x32x16_bf16 v[18:33], v[106:109], v[86:89], v[18:33]
	s_cmp_lg_u64 s[4:5], 0
	s_cbranch_scc0 .LBB3_114
	v_mfma_f32_32x32x16_bf16 v[2:17], v[86:89], v[94:97], v[2:17]
	v_mfma_f32_32x32x16_bf16 v[34:49], v[86:89], v[82:85], v[34:49]
	s_branch .LBB3_116
.LBB3_114:
	v_mfma_f32_32x32x16_bf16 v[2:17], v[94:97], v[86:89], v[2:17]
	v_mfma_f32_32x32x16_bf16 v[34:49], v[82:85], v[86:89], v[34:49]
.LBB3_116:
	s_waitcnt lgkmcnt(3)
	s_barrier
	ds_read_b128 v[86:89], v161 offset:3072
	s_waitcnt lgkmcnt(4)
	ds_read_b128 v[82:85], v161 offset:7168
	ds_read_b128 v[62:65], v161 offset:11264
	s_waitcnt lgkmcnt(3)
	v_mfma_f32_32x32x16_bf16 v[18:33], v[98:101], v[66:69], v[18:33]
	s_cmp_lg_u64 s[4:5], 0
	s_cbranch_scc0 .LBB3_118
	v_mfma_f32_32x32x16_bf16 v[2:17], v[66:69], v[90:93], v[2:17]
	v_mfma_f32_32x32x16_bf16 v[34:49], v[66:69], v[54:57], v[34:49]
	s_branch .LBB3_120
.LBB3_118:
	v_mfma_f32_32x32x16_bf16 v[2:17], v[90:93], v[66:69], v[2:17]
	v_mfma_f32_32x32x16_bf16 v[34:49], v[54:57], v[66:69], v[34:49]
.LBB3_120:
	ds_read_b128 v[66:69], v161 offset:28672
	s_waitcnt lgkmcnt(5)
	ds_read_b128 v[90:93], v161 offset:24576
	s_waitcnt lgkmcnt(5)
	ds_read_b128 v[54:57], v161 offset:32768
	s_waitcnt lgkmcnt(3)
	v_mfma_f32_32x32x16_bf16 v[18:33], v[86:89], v[50:53], v[18:33]
	s_cmp_lg_u64 s[4:5], 0
	s_cbranch_scc0 .LBB3_122
	v_mfma_f32_32x32x16_bf16 v[2:17], v[50:53], v[82:85], v[2:17]
	v_mfma_f32_32x32x16_bf16 v[34:49], v[50:53], v[62:65], v[34:49]
	s_branch .LBB3_124
.LBB3_122:
	v_mfma_f32_32x32x16_bf16 v[2:17], v[82:85], v[50:53], v[2:17]
	v_mfma_f32_32x32x16_bf16 v[34:49], v[62:65], v[50:53], v[34:49]
.LBB3_124:
	s_waitcnt lgkmcnt(4)
	ds_read_b128 v[82:85], v161 offset:29696
	ds_read_b128 v[86:89], v161 offset:25600
	s_waitcnt lgkmcnt(5)
	ds_read_b128 v[62:65], v161 offset:33792
	s_waitcnt vmcnt(3) lgkmcnt(3)
	v_mfma_f32_32x32x16_bf16 v[18:33], v[90:93], v[78:81], v[18:33]
	s_cmp_lg_u64 s[4:5], 0
	s_cbranch_scc0 .LBB3_126
	v_mfma_f32_32x32x16_bf16 v[2:17], v[78:81], v[66:69], v[2:17]
	v_mfma_f32_32x32x16_bf16 v[34:49], v[78:81], v[54:57], v[34:49]
	s_branch .LBB3_128
.LBB3_126:
	v_mfma_f32_32x32x16_bf16 v[2:17], v[66:69], v[78:81], v[2:17]
	v_mfma_f32_32x32x16_bf16 v[34:49], v[54:57], v[78:81], v[34:49]
.LBB3_128:
	s_waitcnt lgkmcnt(3)
	ds_read_b128 v[54:57], v161 offset:30720
	ds_read_b128 v[78:81], v161 offset:26624
	ds_read_b128 v[50:53], v161 offset:34816
	s_waitcnt vmcnt(2) lgkmcnt(3)
	v_mfma_f32_32x32x16_bf16 v[18:33], v[86:89], v[74:77], v[18:33]
	s_cmp_lg_u64 s[4:5], 0
	s_cbranch_scc0 .LBB3_130
	v_mfma_f32_32x32x16_bf16 v[2:17], v[74:77], v[82:85], v[2:17]
	v_mfma_f32_32x32x16_bf16 v[34:49], v[74:77], v[62:65], v[34:49]
	s_branch .LBB3_132
.LBB3_130:
	v_mfma_f32_32x32x16_bf16 v[2:17], v[82:85], v[74:77], v[2:17]
	v_mfma_f32_32x32x16_bf16 v[34:49], v[62:65], v[74:77], v[34:49]
.LBB3_132:
	s_waitcnt lgkmcnt(3)
	s_barrier
	ds_read_b128 v[66:69], v161 offset:31744
	ds_read_b128 v[74:77], v161 offset:27648
	s_waitcnt lgkmcnt(5)
	ds_read_b128 v[62:65], v161 offset:35840
	s_waitcnt vmcnt(1) lgkmcnt(3)
	v_mfma_f32_32x32x16_bf16 v[18:33], v[78:81], v[70:73], v[18:33]
	s_cmp_lg_u64 s[4:5], 0
	s_cbranch_scc0 .LBB3_134
	v_mfma_f32_32x32x16_bf16 v[2:17], v[70:73], v[54:57], v[2:17]
	v_mfma_f32_32x32x16_bf16 v[34:49], v[70:73], v[50:53], v[34:49]
	s_branch .LBB3_136
.LBB3_134:
	v_mfma_f32_32x32x16_bf16 v[2:17], v[54:57], v[70:73], v[2:17]
	v_mfma_f32_32x32x16_bf16 v[34:49], v[50:53], v[70:73], v[34:49]
